# speedup vs baseline: 1.0212x; 1.0071x over previous
_Z4khidPKDF16_PKfS2_S2_S0_PDF16_Pf:
	s_load_dwordx8 s[4:11], s[0:1], 0x0
	s_load_dwordx2 s[12:13], s[0:1], 0x20
	v_lshlrev_b32_e32 v1, 3, v0
	s_lshr_b32 s3, s2, 1
	v_and_b32_e32 v2, 56, v1
	s_and_b32 s15, s3, 0x7ffffffc
	s_lshl_b32 s14, s2, 4
	v_lshlrev_b32_e32 v106, 1, v2
	v_mov_b32_e32 v107, 0
	s_and_b32 s14, s14, 0x70
	v_lshlrev_b32_e32 v126, 2, v2
	s_add_i32 s16, s15, -1
	s_waitcnt lgkmcnt(0)
	v_and_b32_e32 v132, 63, v0
	v_lshlrev_b32_e32 v132, 3, v132
	global_load_dwordx2 v[108:109], v132, s[6:7]
	global_load_dwordx2 v[134:135], v132, s[6:7] offset:512
	global_load_dwordx2 v[136:137], v132, s[6:7] offset:1024
	global_load_dwordx2 v[138:139], v132, s[6:7] offset:1536
	v_lshl_add_u64 v[2:3], s[4:5], 0, v[106:107]
	v_mul_u32_u24_e32 v1, 0x1c8, v0
	s_movk_i32 s4, 0xffee
	v_lshrrev_b32_e32 v114, 3, v0
	s_add_i32 s17, s14, -1
	v_mul_i32_i24_sdwa v4, v1, s4 dst_sel:DWORD dst_unused:UNUSED_PAD src0_sel:WORD_1 src1_sel:DWORD
	v_add_u32_sdwa v124, s16, v1 dst_sel:DWORD dst_unused:UNUSED_PAD src0_sel:DWORD src1_sel:WORD_1
	s_movk_i32 s4, 0x7f
	v_add3_u32 v125, s17, v114, v4
	v_med3_i32 v1, v124, 0, s4
	v_med3_i32 v4, v125, 0, s4
	v_lshlrev_b32_e32 v1, 14, v1
	v_or_b32_e32 v121, 32, v114
	v_lshl_or_b32 v106, v4, 7, v1
	v_mul_lo_u16_e32 v1, 57, v121
	v_lshrrev_b16_e32 v1, 10, v1
	v_mul_i32_i24_e32 v6, 0xffffffee, v1
	v_add_u32_e32 v122, s16, v1
	v_add3_u32 v123, s17, v121, v6
	v_min_u32_e32 v1, 0x7f, v122
	v_med3_i32 v6, v123, 0, s4
	v_lshlrev_b32_e32 v1, 14, v1
	v_or_b32_e32 v118, 64, v114
	v_lshl_add_u64 v[4:5], v[2:3], 0, v[106:107]
	v_lshl_or_b32 v106, v6, 7, v1
	v_mul_lo_u16_e32 v1, 57, v118
	v_lshrrev_b16_e32 v1, 10, v1
	v_lshl_add_u64 v[6:7], v[2:3], 0, v[106:107]
	global_load_dwordx4 v[86:89], v[4:5], off
	global_load_dwordx4 v[82:85], v[6:7], off
	v_mul_i32_i24_e32 v4, 0xffffffee, v1
	v_add_u32_e32 v119, s16, v1
	v_add3_u32 v120, s17, v118, v4
	v_min_u32_e32 v1, 0x7f, v119
	v_med3_i32 v4, v120, 0, s4
	v_lshlrev_b32_e32 v1, 14, v1
	v_or_b32_e32 v115, 0x60, v114
	v_lshl_or_b32 v106, v4, 7, v1
	v_mul_lo_u16_e32 v1, 57, v115
	v_lshrrev_b16_e32 v1, 10, v1
	v_mul_i32_i24_e32 v6, 0xffffffee, v1
	v_add_u32_e32 v116, s16, v1
	v_add3_u32 v117, s17, v115, v6
	v_min_u32_e32 v1, 0x7f, v116
	v_med3_i32 v6, v117, 0, s4
	v_lshlrev_b32_e32 v1, 14, v1
	v_lshrrev_b32_e32 v112, 6, v0
	v_lshl_add_u64 v[4:5], v[2:3], 0, v[106:107]
	v_lshl_or_b32 v106, v6, 7, v1
	v_mul_u32_u24_e32 v1, 0x480, v112
	v_and_b32_e32 v113, 63, v0
	v_lshl_add_u64 v[2:3], v[2:3], 0, v[106:107]
	v_lshlrev_b32_e32 v106, 4, v1
	global_load_dwordx4 v[78:81], v[4:5], off
	global_load_dwordx4 v[74:77], v[2:3], off
	v_lshl_add_u64 v[2:3], s[12:13], 0, v[106:107]
	v_lshlrev_b32_e32 v106, 4, v113
	v_lshl_add_u64 v[2:3], v[2:3], 0, v[106:107]
	s_movk_i32 s4, 0x1000
	v_add_co_u32_e32 v4, vcc, s4, v2
	s_movk_i32 s4, 0x2000
	s_nop 0
	v_addc_co_u32_e32 v5, vcc, 0, v3, vcc
	v_add_co_u32_e32 v90, vcc, s4, v2
	s_movk_i32 s4, 0x3000
	s_nop 0
	v_addc_co_u32_e32 v91, vcc, 0, v3, vcc
	v_add_co_u32_e32 v92, vcc, s4, v2
	s_movk_i32 s4, 0x4000
	s_nop 0
	v_addc_co_u32_e32 v93, vcc, 0, v3, vcc
	v_add_co_u32_e32 v110, vcc, s4, v2
	global_load_dwordx4 v[70:73], v[2:3], off
	global_load_dwordx4 v[66:69], v[2:3], off offset:1024
	v_addc_co_u32_e32 v111, vcc, 0, v3, vcc
	global_load_dwordx4 v[62:65], v[2:3], off offset:2048
	global_load_dwordx4 v[58:61], v[2:3], off offset:3072
	global_load_dwordx4 v[50:53], v[4:5], off offset:1024
	global_load_dwordx4 v[46:49], v[4:5], off offset:2048
	global_load_dwordx4 v[42:45], v[4:5], off offset:3072
	global_load_dwordx4 v[18:21], v[92:93], off offset:1024
	global_load_dwordx4 v[14:17], v[92:93], off offset:2048
	global_load_dwordx4 v[10:13], v[92:93], off offset:3072
	global_load_dwordx4 v[54:57], v[90:91], off offset:-4096
	global_load_dwordx4 v[38:41], v[90:91], off
	global_load_dwordx4 v[34:37], v[90:91], off offset:1024
	global_load_dwordx4 v[30:33], v[90:91], off offset:2048
	global_load_dwordx4 v[26:29], v[90:91], off offset:3072
	global_load_dwordx4 v[22:25], v[110:111], off offset:-4096
	global_load_dwordx4 v[6:9], v[110:111], off
	s_nop 0
	global_load_dwordx4 v[2:5], v[110:111], off offset:1024
	global_load_dwordx4 v[94:97], v126, s[8:9] offset:16
	global_load_dwordx4 v[90:93], v126, s[10:11] offset:16
	global_load_dwordx4 v[102:105], v126, s[8:9]
	global_load_dwordx4 v[98:101], v126, s[10:11]
	v_cmp_eq_u32_e64 s[4:5], 63, v113
	s_waitcnt vmcnt(26)
	v_pk_add_f32 v[108:109], v[108:109], v[134:135]
	v_pk_add_f32 v[136:137], v[136:137], v[138:139]
	v_pk_add_f32 v[108:109], v[108:109], v[136:137]
	s_nop 1
	v_mov_b32_dpp v110, v108 row_shr:1 row_mask:0xf bank_mask:0xf bound_ctrl:1
	v_mov_b32_dpp v111, v109 row_shr:1 row_mask:0xf bank_mask:0xf bound_ctrl:1
	v_pk_add_f32 v[108:109], v[108:109], v[110:111]
	v_lshlrev_b32_e32 v1, 3, v112
	s_nop 0
	v_mov_b32_dpp v110, v108 row_shr:2 row_mask:0xf bank_mask:0xf bound_ctrl:1
	v_mov_b32_dpp v111, v109 row_shr:2 row_mask:0xf bank_mask:0xf bound_ctrl:1
	v_pk_add_f32 v[108:109], v[108:109], v[110:111]
	s_nop 1
	v_mov_b32_dpp v110, v108 row_shr:4 row_mask:0xf bank_mask:0xf bound_ctrl:1
	v_mov_b32_dpp v111, v109 row_shr:4 row_mask:0xf bank_mask:0xf bound_ctrl:1
	v_pk_add_f32 v[108:109], v[108:109], v[110:111]
	s_nop 1
	v_mov_b32_dpp v110, v108 row_shr:8 row_mask:0xf bank_mask:0xf bound_ctrl:1
	v_mov_b32_dpp v111, v109 row_shr:8 row_mask:0xf bank_mask:0xf bound_ctrl:1
	v_pk_add_f32 v[108:109], v[108:109], v[110:111]
	v_mov_b32_e32 v110, v107
	v_mov_b32_e32 v111, v107
	s_nop 0
	v_mov_b32_dpp v110, v108 row_bcast:15 row_mask:0xa bank_mask:0xf
	v_mov_b32_dpp v111, v109 row_bcast:15 row_mask:0xa bank_mask:0xf
	v_pk_add_f32 v[108:109], v[108:109], v[110:111]
	v_mov_b32_e32 v110, 0
	v_mov_b32_e32 v111, 0
	s_nop 0
	v_mov_b32_dpp v110, v108 row_bcast:31 row_mask:0xc bank_mask:0xf
	v_mov_b32_dpp v111, v109 row_bcast:31 row_mask:0xc bank_mask:0xf
	v_pk_add_f32 v[108:109], v[108:109], v[110:111]
	s_mov_b32 s6, 0xf800000
	s_nop 0
	v_readlane_b32 s18, v108, 63
	v_readlane_b32 s19, v109, 63
	s_nop 3
	v_mov_b32_e32 v106, s18
	v_mov_b32_e32 v107, s19
	v_mul_f32_e32 v109, 0x35800000, v106
	v_mul_f32_e32 v106, 0x35800000, v107
	v_fma_f32 v106, -v109, v109, v106
	v_add_f32_e32 v106, 0x3727c5ac, v106
	v_mul_f32_e32 v107, 0x4f800000, v106
	v_cmp_gt_f32_e32 vcc, s6, v106
	s_nop 1
	v_cndmask_b32_e32 v106, v106, v107, vcc
	v_sqrt_f32_e32 v107, v106
	s_nop 0
	v_add_u32_e32 v108, -1, v107
	v_fma_f32 v110, -v108, v107, v106
	v_cmp_ge_f32_e64 s[6:7], 0, v110
	v_add_u32_e32 v110, 1, v107
	s_nop 0
	v_cndmask_b32_e64 v108, v107, v108, s[6:7]
	v_fma_f32 v107, -v110, v107, v106
	v_cmp_lt_f32_e64 s[6:7], 0, v107
	s_nop 1
	v_cndmask_b32_e64 v107, v108, v110, s[6:7]
	v_mul_f32_e32 v108, 0x37800000, v107
	v_cndmask_b32_e32 v107, v107, v108, vcc
	v_mov_b32_e32 v108, 0x260
	v_cmp_class_f32_e32 vcc, v106, v108
	s_nop 1
	v_cndmask_b32_e32 v106, v107, v106, vcc
	v_div_scale_f32 v107, s[6:7], v106, v106, 1.0
	v_rcp_f32_e32 v108, v107
	s_movk_i32 s6, 0x360
	v_cmp_gt_u32_e64 s[6:7], s6, v0
	v_fma_f32 v110, -v107, v108, 1.0
	v_fmac_f32_e32 v108, v110, v108
	v_div_scale_f32 v110, vcc, 1.0, v106, 1.0
	v_mul_f32_e32 v111, v110, v108
	v_fma_f32 v126, -v107, v111, v110
	v_fmac_f32_e32 v111, v126, v108
	v_fma_f32 v107, -v107, v111, v110
	v_div_fmas_f32 v107, v107, v108, v111
	v_div_fixup_f32 v110, v107, v106, 1.0
	s_waitcnt vmcnt(1)
	v_mul_f32_e32 v102, v110, v102
	v_mul_f32_e32 v94, v110, v94
	s_waitcnt vmcnt(0)
	v_fma_f32 v106, -v109, v102, v98
	v_fma_f32 v98, -v109, v94, v90
	v_mul_f32_e32 v107, v110, v103
	v_mul_f32_e32 v95, v110, v95
	v_xor_b32_e32 v90, v114, v0
	v_fma_f32 v108, -v109, v107, v99
	v_fma_f32 v99, -v109, v95, v91
	v_mul_f32_e32 v103, v110, v104
	v_mul_f32_e32 v91, v110, v96
	v_mul_f32_e32 v104, v110, v105
	v_mul_f32_e32 v96, v110, v97
	v_lshlrev_b32_e32 v90, 4, v90
	v_fma_f32 v100, -v109, v103, v100
	v_fma_f32 v92, -v109, v91, v92
	v_fma_f32 v97, -v109, v104, v101
	v_fma_f32 v93, -v109, v96, v93
	v_and_b32_e32 v90, 0x70, v90
	v_fma_mixlo_f16 v101, v86, v102, v106 op_sel_hi:[1,0,0]
	v_fma_mixhi_f16 v101, v86, v107, v108 op_sel:[1,0,0] op_sel_hi:[1,0,0]
	v_pk_max_f16 v101, v101, 0
	v_fma_mixlo_f16 v86, v87, v103, v100 op_sel_hi:[1,0,0]
	v_fma_mixhi_f16 v86, v87, v104, v97 op_sel:[1,0,0] op_sel_hi:[1,0,0]
	v_pk_max_f16 v86, v86, 0
	v_fma_mixlo_f16 v87, v88, v94, v98 op_sel_hi:[1,0,0]
	v_fma_mixhi_f16 v87, v88, v95, v99 op_sel:[1,0,0] op_sel_hi:[1,0,0]
	v_pk_max_f16 v87, v87, 0
	v_fma_mixlo_f16 v88, v89, v91, v92 op_sel_hi:[1,0,0]
	v_fma_mixhi_f16 v88, v89, v96, v93 op_sel:[1,0,0] op_sel_hi:[1,0,0]
	v_pk_max_f16 v88, v88, 0
	s_and_saveexec_b64 s[8:9], s[6:7]
	s_cbranch_execz .LBB1_4
	v_or_b32_e32 v89, v125, v124
	s_movk_i32 s6, 0x80
	v_cmp_gt_u32_e32 vcc, s6, v89
	v_lshl_or_b32 v105, v114, 7, v90
	s_nop 0
	v_cndmask_b32_e32 v89, 0, v88, vcc
	v_cndmask_b32_e32 v88, 0, v87, vcc
	v_cndmask_b32_e32 v87, 0, v86, vcc
	v_cndmask_b32_e32 v86, 0, v101, vcc
	ds_write_b128 v105, v[86:89]

	.amdhsa_kernel _Z4khidPKDF16_PKfS2_S2_S0_PDF16_Pf
		.amdhsa_group_segment_fixed_size 14112
		.amdhsa_private_segment_fixed_size 0
		.amdhsa_kernarg_size 56
		.amdhsa_user_sgpr_count 2
		.amdhsa_user_sgpr_dispatch_ptr 0
		.amdhsa_user_sgpr_queue_ptr 0
		.amdhsa_user_sgpr_kernarg_segment_ptr 1
		.amdhsa_user_sgpr_dispatch_id 0
		.amdhsa_user_sgpr_kernarg_preload_length 0
		.amdhsa_user_sgpr_kernarg_preload_offset 0
		.amdhsa_user_sgpr_private_segment_size 0
		.amdhsa_uses_dynamic_stack 0
		.amdhsa_enable_private_segment 0
		.amdhsa_system_sgpr_workgroup_id_x 1
		.amdhsa_system_sgpr_workgroup_id_y 0
		.amdhsa_system_sgpr_workgroup_id_z 0
		.amdhsa_system_sgpr_workgroup_info 0
		.amdhsa_system_vgpr_workitem_id 0
		.amdhsa_next_free_vgpr 156
		.amdhsa_next_free_sgpr 20
		.amdhsa_accum_offset 140
		.amdhsa_reserve_vcc 1
		.amdhsa_float_round_mode_32 0
		.amdhsa_float_round_mode_16_64 0
		.amdhsa_float_denorm_mode_32 3
		.amdhsa_float_denorm_mode_16_64 3
		.amdhsa_dx10_clamp 1
		.amdhsa_ieee_mode 1
		.amdhsa_fp16_overflow 0
		.amdhsa_tg_split 0
		.amdhsa_exception_fp_ieee_invalid_op 0
		.amdhsa_exception_fp_denorm_src 0
		.amdhsa_exception_fp_ieee_div_zero 0
		.amdhsa_exception_fp_ieee_overflow 0
		.amdhsa_exception_fp_ieee_underflow 0
		.amdhsa_exception_fp_ieee_inexact 0
		.amdhsa_exception_int_div_zero 0
	.end_amdhsa_kernel

amdhsa.kernels:
  - .agpr_count:     0
    .args:
      - .actual_access:  read_only
        .address_space:  global
        .offset:         0
        .size:           8
        .value_kind:     global_buffer
      - .actual_access:  read_only
        .address_space:  global
        .offset:         8
        .size:           8
        .value_kind:     global_buffer
      - .actual_access:  read_only
        .address_space:  global
        .offset:         16
        .size:           8
        .value_kind:     global_buffer
      - .actual_access:  read_only
        .address_space:  global
        .offset:         24
        .size:           8
        .value_kind:     global_buffer
      - .actual_access:  read_only
        .address_space:  global
        .offset:         32
        .size:           8
        .value_kind:     global_buffer
      - .actual_access:  read_only
        .address_space:  global
        .offset:         40
        .size:           8
        .value_kind:     global_buffer
      - .actual_access:  write_only
        .address_space:  global
        .offset:         48
        .size:           8
        .value_kind:     global_buffer
      - .actual_access:  write_only
        .address_space:  global
        .offset:         56
        .size:           8
        .value_kind:     global_buffer
      - .actual_access:  write_only
        .address_space:  global
        .offset:         64
        .size:           8
        .value_kind:     global_buffer
      - .actual_access:  write_only
        .address_space:  global
        .offset:         72
        .size:           8
        .value_kind:     global_buffer
    .group_segment_fixed_size: 12000
    .kernarg_segment_align: 8
    .kernarg_segment_size: 80
    .language:       OpenCL C
    .language_version:
      - 2
      - 0
    .max_flat_workgroup_size: 256
    .name:           _Z2k0PKfS0_S0_S0_S0_S0_PDF16_PfS1_S1_
    .private_segment_fixed_size: 0
    .sgpr_count:     24
    .sgpr_spill_count: 0
    .symbol:         _Z2k0PKfS0_S0_S0_S0_S0_PDF16_PfS1_S1_.kd
    .uniform_work_group_size: 1
    .uses_dynamic_stack: false
    .vgpr_count:     150
    .vgpr_spill_count: 0
    .wavefront_size: 64
  - .agpr_count:     16
    .args:
      - .actual_access:  read_only
        .address_space:  global
        .offset:         0
        .size:           8
        .value_kind:     global_buffer
      - .actual_access:  read_only
        .address_space:  global
        .offset:         8
        .size:           8
        .value_kind:     global_buffer
      - .actual_access:  read_only
        .address_space:  global
        .offset:         16
        .size:           8
        .value_kind:     global_buffer
      - .actual_access:  read_only
        .address_space:  global
        .offset:         24
        .size:           8
        .value_kind:     global_buffer
      - .actual_access:  read_only
        .address_space:  global
        .offset:         32
        .size:           8
        .value_kind:     global_buffer
      - .actual_access:  write_only
        .address_space:  global
        .offset:         40
        .size:           8
        .value_kind:     global_buffer
      - .actual_access:  write_only
        .address_space:  global
        .offset:         48
        .size:           8
        .value_kind:     global_buffer
    .group_segment_fixed_size: 14112
    .kernarg_segment_align: 8
    .kernarg_segment_size: 56
    .language:       OpenCL C
    .language_version:
      - 2
      - 0
    .max_flat_workgroup_size: 256
    .name:           _Z4khidPKDF16_PKfS2_S2_S0_PDF16_Pf
    .private_segment_fixed_size: 0
    .sgpr_count:     26
    .sgpr_spill_count: 0
    .symbol:         _Z4khidPKDF16_PKfS2_S2_S0_PDF16_Pf.kd
    .uniform_work_group_size: 1
    .uses_dynamic_stack: false
    .vgpr_count:     156
    .vgpr_spill_count: 0
    .wavefront_size: 64
  - .agpr_count:     144
    .args:
      - .actual_access:  read_only
        .address_space:  global
        .offset:         0
        .size:           8
        .value_kind:     global_buffer
      - .actual_access:  read_only
        .address_space:  global
        .offset:         8
        .size:           8
        .value_kind:     global_buffer
      - .actual_access:  read_only
        .address_space:  global
        .offset:         16
        .size:           8
        .value_kind:     global_buffer
      - .actual_access:  read_only
        .address_space:  global
        .offset:         24
        .size:           8
        .value_kind:     global_buffer
      - .address_space:  global
        .offset:         32
        .size:           8
        .value_kind:     global_buffer
      - .address_space:  global
        .offset:         40
        .size:           8
        .value_kind:     global_buffer
      - .address_space:  global
        .offset:         48
        .size:           8
        .value_kind:     global_buffer
    .group_segment_fixed_size: 0
    .kernarg_segment_align: 8
    .kernarg_segment_size: 56
    .language:       OpenCL C
    .language_version:
      - 2
      - 0
    .max_flat_workgroup_size: 256
    .name:           _Z6kfinalPKDF16_PKfS2_S2_PK15HIP_vector_typeIjLj4EES2_Pf
    .private_segment_fixed_size: 0
    .sgpr_count:     41
    .sgpr_spill_count: 0
    .symbol:         _Z6kfinalPKDF16_PKfS2_S2_PK15HIP_vector_typeIjLj4EES2_Pf.kd
    .uniform_work_group_size: 1
    .uses_dynamic_stack: false
    .vgpr_count:     400
    .vgpr_spill_count: 0
    .wavefront_size: 64
  - .agpr_count:     73
    .args:
      - .actual_access:  read_only
        .address_space:  global
        .offset:         0
        .size:           8
        .value_kind:     global_buffer
      - .actual_access:  read_only
        .address_space:  global
        .offset:         8
        .size:           8
        .value_kind:     global_buffer
      - .actual_access:  read_only
        .address_space:  global
        .offset:         16
        .size:           8
        .value_kind:     global_buffer
      - .actual_access:  read_only
        .address_space:  global
        .offset:         24
        .size:           8
        .value_kind:     global_buffer
      - .address_space:  global
        .offset:         32
        .size:           8
        .value_kind:     global_buffer
      - .address_space:  global
        .offset:         40
        .size:           8
        .value_kind:     global_buffer
      - .address_space:  global
        .offset:         48
        .size:           8
        .value_kind:     global_buffer
    .group_segment_fixed_size: 0
    .kernarg_segment_align: 8
    .kernarg_segment_size: 56
    .language:       OpenCL C
    .language_version:
      - 2
      - 0
    .max_flat_workgroup_size: 512
    .name:           _Z7kfinal3PKDF16_PKfS2_S2_PK15HIP_vector_typeIjLj4EES2_Pf
    .private_segment_fixed_size: 0
    .sgpr_count:     60
    .sgpr_spill_count: 0
    .symbol:         _Z7kfinal3PKDF16_PKfS2_S2_PK15HIP_vector_typeIjLj4EES2_Pf.kd
    .uniform_work_group_size: 1
    .uses_dynamic_stack: false
    .vgpr_count:     245
    .vgpr_spill_count: 0
    .wavefront_size: 64
